# P5 loader: exec-mask diamonds replaced by v_cndmask pointer select (on top of bf16 p copy + static prio)
# speedup vs baseline: 1.0118x; 1.0044x over previous
.LBB0_1548:
	s_lshl_b32 s40, s56, 7
	v_mov_b32_e32 v92, v0
	s_waitcnt vmcnt(0)
	s_waitcnt lgkmcnt(0)
	s_barrier
	s_ashr_i32 s41, s40, 31
	s_lshl_b64 s[0:1], s[40:41], 10
	v_ashrrev_i32_e32 v84, 4, v92
	v_add_u32_e32 v86, 32, v84
	v_add_u32_e32 v88, 64, v84
	s_add_u32 s0, s53, s0
	v_lshlrev_b32_e32 v4, 3, v92
	v_ashrrev_i32_e32 v85, 31, v84
	v_ashrrev_i32_e32 v87, 31, v86
	v_ashrrev_i32_e32 v89, 31, v88
	s_addc_u32 s1, s54, s1
	v_and_b32_e32 v165, 0x78, v4
	v_lshlrev_b64 v[4:5], 10, v[84:85]
	v_lshlrev_b64 v[12:13], 10, v[86:87]
	v_lshlrev_b64 v[20:21], 10, v[88:89]
	v_lshl_add_u64 v[168:169], s[0:1], 0, v[4:5]
	v_lshlrev_b32_e32 v28, 2, v165
	v_mov_b32_e32 v29, v2
	v_lshl_add_u64 v[170:171], s[0:1], 0, v[12:13]
	v_lshl_add_u64 v[172:173], s[0:1], 0, v[20:21]
	v_lshl_add_u64 v[40:41], v[168:169], 0, v[28:29]
	v_lshl_add_u64 v[48:49], v[170:171], 0, v[28:29]
	v_lshl_add_u64 v[56:57], v[172:173], 0, v[28:29]
	global_load_dwordx4 v[4:7], v[40:41], off offset:16
	global_load_dwordx4 v[8:11], v[40:41], off
	global_load_dwordx4 v[12:15], v[48:49], off offset:16
	global_load_dwordx4 v[16:19], v[48:49], off
	global_load_dwordx4 v[20:23], v[56:57], off offset:16
	global_load_dwordx4 v[24:27], v[56:57], off
	v_add_u32_e32 v90, 0x60, v84
	v_ashrrev_i32_e32 v91, 31, v90
	v_lshlrev_b64 v[30:31], 10, v[90:91]
	v_lshl_add_u64 v[174:175], s[0:1], 0, v[30:31]
	v_lshl_add_u64 v[64:65], v[174:175], 0, v[28:29]
	v_readlane_b32 s0, v251, 59
	v_readlane_b32 s1, v251, 60
	v_lshlrev_b32_e32 v168, 9, v84
	v_mov_b32_e32 v169, v2
	v_lshlrev_b32_e32 v244, 1, v165
	v_mov_b32_e32 v245, v2
	v_lshl_add_u64 v[168:169], s[0:1], 0, v[168:169]
	s_mov_b64 s[0:1], 0x4000
	v_lshl_add_u64 v[170:171], v[168:169], 0, s[0:1]
	s_mov_b64 s[0:1], 0x8000
	v_lshl_add_u64 v[172:173], v[168:169], 0, s[0:1]
	s_mov_b64 s[0:1], 0xc000
	v_lshl_add_u64 v[174:175], v[168:169], 0, s[0:1]
	v_lshl_add_u64 v[236:237], v[168:169], 0, v[244:245]
	v_lshl_add_u64 v[238:239], v[170:171], 0, v[244:245]
	v_lshl_add_u64 v[240:241], v[172:173], 0, v[244:245]
	v_lshl_add_u64 v[242:243], v[174:175], 0, v[244:245]
	s_mov_b64 s[0:1], 0x200
	v_lshl_add_u64 v[168:169], v[168:169], 0, s[0:1]
	v_lshl_add_u64 v[170:171], v[170:171], 0, s[0:1]
	v_lshl_add_u64 v[172:173], v[172:173], 0, s[0:1]
	v_lshl_add_u64 v[174:175], v[174:175], 0, s[0:1]
	global_load_dwordx4 v[28:31], v[64:65], off
	global_load_dwordx4 v[32:35], v[64:65], off offset:16
	global_load_dwordx4 v[36:39], v[40:41], off offset:512
	s_nop 0
	global_load_dwordx4 v[40:43], v[40:41], off offset:528
	s_nop 0
	global_load_dwordx4 v[44:47], v[48:49], off offset:512
	s_nop 0
	global_load_dwordx4 v[48:51], v[48:49], off offset:528
	s_nop 0
	global_load_dwordx4 v[52:55], v[56:57], off offset:512
	s_nop 0
	global_load_dwordx4 v[56:59], v[56:57], off offset:528
	s_nop 0
	global_load_dwordx4 v[60:63], v[64:65], off offset:512
	s_nop 0
	global_load_dwordx4 v[64:67], v[64:65], off offset:528
	s_lshl_b64 s[0:1], s[40:41], 11
	v_readfirstlane_b32 s12, v92
	s_add_u32 s0, s8, s0
	s_addc_u32 s1, s9, s1
	s_ashr_i32 s12, s12, 6
	s_cmp_lt_i32 s12, 8
	s_cselect_b64 s[38:39], -1, 0
	s_and_b64 s[42:43], s[38:39], exec
	s_cselect_b32 s41, s12, 7
	s_mul_hi_i32 s43, s41, 0x14000
	s_mul_i32 s41, s41, 0x14000
	v_and_b32_e32 v68, 63, v92
	s_add_u32 s42, s20, s41
	v_readlane_b32 s18, v248, 29
	v_mov_b32_e32 v69, v2
	v_lshlrev_b32_e32 v68, 4, v68
	s_addc_u32 s43, s52, s43
	v_readlane_b32 s19, v248, 30
	v_xor_b32_e32 v71, v84, v92
	v_lshl_add_u64 v[176:177], s[42:43], 0, v[68:69]
	s_mov_b32 s19, s21
	v_lshlrev_b32_e32 v70, 8, v84
	v_lshlrev_b32_e32 v71, 4, v71
	v_and_or_b32 v93, v71, s84, v70
	v_bfe_u32 v192, v92, 4, 2
	v_and_b32_e32 v167, 15, v92
	v_add_u32_e32 v193, 0, v93
	s_lshl_b32 s42, s12, 13
	s_lshl_b32 s41, s12, 5
	s_lshl_b32 s12, s12, 9
	s_mov_b32 s26, s18
	s_add_i32 s48, s42, 0
	s_add_i32 s49, s12, 0
	s_mov_b32 s60, 2
	s_mov_b32 s58, 1
	v_writelane_b32 v248, s26, 29
	s_mov_b32 s59, 0
	s_ashr_i32 s47, s41, 31
	s_add_i32 s48, s48, 0x10000
	s_add_i32 s49, s49, 0x20000
	s_mov_b32 s50, -2
	s_mov_b32 s51, 0
	s_mov_b32 s42, 0
	v_writelane_b32 v248, s27, 30
	s_waitcnt vmcnt(9)
	v_cvt_pk_bf16_f32 v80, v28, v29
	s_waitcnt vmcnt(8)
	v_cvt_pk_bf16_f32 v82, v32, v33
	v_lshl_add_u64 v[32:33], v[176:177], 0, s[18:19]
	v_cvt_pk_bf16_f32 v71, v6, v7
	v_cvt_pk_bf16_f32 v76, v24, v25
	v_cvt_pk_bf16_f32 v77, v26, v27
	v_cvt_pk_bf16_f32 v78, v20, v21
	v_cvt_pk_bf16_f32 v79, v22, v23
	v_cvt_pk_bf16_f32 v81, v30, v31
	s_waitcnt vmcnt(6)
	v_cvt_pk_bf16_f32 v6, v40, v41
	v_cvt_pk_bf16_f32 v7, v42, v43
	global_load_dwordx4 v[40:43], v[32:33], off
	global_load_dwordx4 v[28:31], v[32:33], off offset:1024
	global_load_dwordx4 v[24:27], v[32:33], off offset:2048
	global_load_dwordx4 v[20:23], v[32:33], off offset:3072
	v_add_co_u32_e32 v32, vcc, s22, v32
	v_cvt_pk_bf16_f32 v68, v8, v9
	s_nop 0
	v_addc_co_u32_e32 v33, vcc, 0, v33, vcc
	v_cvt_pk_bf16_f32 v69, v10, v11
	v_cvt_pk_bf16_f32 v70, v4, v5
	v_cvt_pk_bf16_f32 v74, v12, v13
	v_cvt_pk_bf16_f32 v4, v36, v37
	v_cvt_pk_bf16_f32 v5, v38, v39
	s_waitcnt vmcnt(9)
	v_cvt_pk_bf16_f32 v8, v44, v45
	v_cvt_pk_bf16_f32 v9, v46, v47
	s_waitcnt vmcnt(8)
	v_cvt_pk_bf16_f32 v10, v48, v49
	v_cvt_pk_bf16_f32 v11, v50, v51
	s_waitcnt vmcnt(7)
	v_cvt_pk_bf16_f32 v12, v52, v53
	v_cvt_pk_bf16_f32 v13, v54, v55
	global_load_dwordx4 v[52:55], v[32:33], off
	global_load_dwordx4 v[48:51], v[32:33], off offset:1024
	global_load_dwordx4 v[44:47], v[32:33], off offset:2048
	global_load_dwordx4 v[36:39], v[32:33], off offset:3072
	v_bitop3_b32 v32, v192, v92, 15 bitop3:0x78
	v_cvt_pk_bf16_f32 v83, v34, v35
	v_lshlrev_b32_e32 v35, 4, v32
	v_bitop3_b32 v32, v192, v167, 4 bitop3:0x36
	v_cvt_pk_bf16_f32 v75, v14, v15
	s_waitcnt vmcnt(10)
	v_cvt_pk_bf16_f32 v14, v56, v57
	v_lshlrev_b32_e32 v56, 4, v32
	v_bitop3_b32 v32, v192, v167, 8 bitop3:0x36
	v_lshlrev_b32_e32 v57, 4, v32
	v_bitop3_b32 v32, v192, v167, 12 bitop3:0x36
	v_cvt_pk_bf16_f32 v15, v58, v59
	v_lshlrev_b32_e32 v58, 4, v32
	v_lshlrev_b64 v[32:33], 11, v[84:85]
	v_lshl_add_u64 v[178:179], s[0:1], 0, v[32:33]
	v_lshlrev_b64 v[32:33], 11, v[86:87]
	v_lshl_add_u64 v[180:181], s[0:1], 0, v[32:33]
	v_lshlrev_b64 v[32:33], 11, v[88:89]
	v_cvt_pk_bf16_f32 v72, v16, v17
	v_cvt_pk_bf16_f32 v73, v18, v19
	global_store_dwordx4 v[236:237], v[68:71], off
	global_store_dwordx4 v[238:239], v[72:75], off
	global_store_dwordx4 v[240:241], v[76:79], off
	global_store_dwordx4 v[242:243], v[80:83], off
	ds_write_b128 v193, v[68:71]
	ds_write_b128 v193, v[72:75] offset:8192
	ds_write_b128 v193, v[76:79] offset:16384
	ds_write_b128 v193, v[80:83] offset:24576
	v_lshl_add_u32 v34, v167, 8, 0
	v_lshl_add_u64 v[182:183], s[0:1], 0, v[32:33]
	v_lshlrev_b64 v[32:33], 11, v[90:91]
	v_mov_b32_e32 v68, 0
	s_waitcnt vmcnt(13)
	v_cvt_pk_bf16_f32 v16, v60, v61
	v_cvt_pk_bf16_f32 v17, v62, v63
	s_waitcnt vmcnt(12)
	v_cvt_pk_bf16_f32 v18, v64, v65
	v_cvt_pk_bf16_f32 v19, v66, v67
	global_store_dwordx4 v[236:237], v[4:7], off offset:256
	global_store_dwordx4 v[238:239], v[8:11], off offset:256
	global_store_dwordx4 v[240:241], v[12:15], off offset:256
	global_store_dwordx4 v[242:243], v[16:19], off offset:256
	v_lshl_add_u64 v[184:185], s[0:1], 0, v[32:33]
	v_add_u32_e32 v194, v34, v35
	v_add_u32_e32 v195, v34, v56
	v_add_u32_e32 v196, v34, v57
	v_add_u32_e32 v197, v34, v58
	v_mov_b32_e32 v69, v68
	v_mov_b32_e32 v70, v68
	v_mov_b32_e32 v71, v68
	v_mov_b32_e32 v72, v68
	v_mov_b32_e32 v73, v68
	v_mov_b32_e32 v74, v68
	v_mov_b32_e32 v75, v68
	v_mov_b32_e32 v76, v68
	v_mov_b32_e32 v77, v68
	v_mov_b32_e32 v78, v68
	v_mov_b32_e32 v79, v68
	v_mov_b32_e32 v84, v68
	v_mov_b32_e32 v85, v68
	v_mov_b32_e32 v86, v68
	v_mov_b32_e32 v87, v68
	v_mov_b32_e32 v88, v68
	v_mov_b32_e32 v89, v68
	v_mov_b32_e32 v90, v68
	v_mov_b32_e32 v91, v68
	v_mov_b32_e32 v92, v68
	v_mov_b32_e32 v93, v68
	v_mov_b32_e32 v94, v68
	v_mov_b32_e32 v95, v68
	v_mov_b32_e32 v96, v68
	v_mov_b32_e32 v97, v68
	v_mov_b32_e32 v98, v68
	v_mov_b32_e32 v99, v68
	v_mov_b32_e32 v100, v68
	v_mov_b32_e32 v101, v68
	v_mov_b32_e32 v102, v68
	v_mov_b32_e32 v103, v68
	v_mov_b32_e32 v60, v68
	v_mov_b32_e32 v61, v68
	v_mov_b32_e32 v62, v68
	v_mov_b32_e32 v63, v68
	v_mov_b32_e32 v64, v68
	v_mov_b32_e32 v65, v68
	v_mov_b32_e32 v66, v68
	v_mov_b32_e32 v67, v68
	v_mov_b32_e32 v104, v68
	v_mov_b32_e32 v105, v68
	v_mov_b32_e32 v106, v68
	v_mov_b32_e32 v107, v68
	v_mov_b32_e32 v108, v68
	v_mov_b32_e32 v109, v68
	v_mov_b32_e32 v110, v68
	v_mov_b32_e32 v111, v68
	v_mov_b32_e32 v116, v68
	v_mov_b32_e32 v117, v68
	v_mov_b32_e32 v118, v68
	v_mov_b32_e32 v119, v68
	v_mov_b32_e32 v120, v68
	v_mov_b32_e32 v121, v68
	v_mov_b32_e32 v122, v68
	v_mov_b32_e32 v123, v68
	v_mov_b32_e32 v132, v68
	v_mov_b32_e32 v133, v68
	v_mov_b32_e32 v134, v68
	v_mov_b32_e32 v135, v68
	v_mov_b32_e32 v136, v68
	v_mov_b32_e32 v137, v68
	v_mov_b32_e32 v138, v68
	v_mov_b32_e32 v139, v68
	s_waitcnt lgkmcnt(0)
	s_barrier
	s_branch .LBB0_1552

.LBB0_1556:
	ds_read_b128 v[152:155], v194
	ds_read_b128 v[148:151], v194 offset:4096
	ds_read_b128 v[140:143], v194 offset:8192
	ds_read_b128 v[144:147], v194 offset:12288
	ds_read_b128 v[128:131], v194 offset:16384
	ds_read_b128 v[124:127], v194 offset:20480
	ds_read_b128 v[112:115], v194 offset:24576
	ds_read_b128 v[80:83], v194 offset:28672
	s_lshl_b32 s0, s60, 7
	s_add_i32 s1, s0, 0xfffffb00
	s_cmp_gt_i32 s60, 9
	s_cselect_b32 s0, s1, s0
	v_or_b32_e32 v186, s0, v165
	s_movk_i32 s0, 0xff
	v_cmp_lt_i32_e32 vcc, s0, v186
	v_mov_b32_e32 v187, v2
	s_nop 0
	v_cndmask_b32_e32 v32, v168, v178, vcc
	v_cndmask_b32_e32 v33, v169, v179, vcc
	v_lshl_add_u64 v[32:33], v[186:187], 1, v[32:33]
	global_load_dwordx4 v[32:35], v[32:33], off offset:-512
	v_cndmask_b32_e32 v56, v170, v180, vcc
	v_cndmask_b32_e32 v57, v171, v181, vcc
	v_lshl_add_u64 v[56:57], v[186:187], 1, v[56:57]
	global_load_dwordx4 v[56:59], v[56:57], off offset:-512
	s_waitcnt vmcnt(7) lgkmcnt(7)
	v_mfma_f32_16x16x32_bf16 v[136:139], v[40:43], v[152:155], v[136:139]
	s_waitcnt vmcnt(3)
	v_mfma_f32_16x16x32_bf16 v[132:135], v[52:55], v[152:155], v[132:135]
	s_waitcnt lgkmcnt(6)
	v_mfma_f32_16x16x32_bf16 v[120:123], v[40:43], v[148:151], v[120:123]
	v_mfma_f32_16x16x32_bf16 v[116:119], v[52:55], v[148:151], v[116:119]
	s_waitcnt lgkmcnt(5)
	v_mfma_f32_16x16x32_bf16 v[108:111], v[40:43], v[140:143], v[108:111]
	v_mfma_f32_16x16x32_bf16 v[104:107], v[52:55], v[140:143], v[104:107]
	s_waitcnt lgkmcnt(4)
	v_mfma_f32_16x16x32_bf16 v[140:143], v[40:43], v[144:147], v[64:67]
	v_mfma_f32_16x16x32_bf16 v[144:147], v[52:55], v[144:147], v[60:63]
	ds_read_b128 v[160:163], v195
	ds_read_b128 v[156:159], v195 offset:4096
	ds_read_b128 v[152:155], v195 offset:8192
	ds_read_b128 v[148:151], v195 offset:12288
	v_cndmask_b32_e32 v60, v172, v182, vcc
	v_cndmask_b32_e32 v61, v173, v183, vcc
	v_lshl_add_u64 v[60:61], v[186:187], 1, v[60:61]
	global_load_dwordx4 v[60:63], v[60:61], off offset:-512
	v_cndmask_b32_e32 v64, v174, v184, vcc
	v_cndmask_b32_e32 v65, v175, v185, vcc
	v_lshl_add_u64 v[64:65], v[186:187], 1, v[64:65]
	global_load_dwordx4 v[64:67], v[64:65], off offset:-512
	s_add_i32 s0, s59, s23
	s_add_i32 s1, s0, -4
	s_cmp_gt_i32 s0, 3
	s_cselect_b32 s0, s1, s0
	s_lshl_b32 s1, s58, 2
	s_sub_i32 s12, s1, 40
	s_cmp_gt_i32 s58, 9
	s_cselect_b32 s1, s12, s1
	s_mul_hi_i32 s43, s0, 0x280
	s_mulk_i32 s0, 0x280
	s_ashr_i32 s12, s1, 31
	s_add_u32 s0, s0, s1
	s_addc_u32 s1, s43, s12
	s_lshl_b64 s[0:1], s[0:1], 10
	v_lshl_add_u64 v[186:187], v[176:177], 0, s[0:1]
	s_waitcnt lgkmcnt(7)
	v_mfma_f32_16x16x32_bf16 v[100:103], v[40:43], v[128:131], v[100:103]
	v_mfma_f32_16x16x32_bf16 v[96:99], v[52:55], v[128:131], v[96:99]
	s_waitcnt lgkmcnt(6)
	v_mfma_f32_16x16x32_bf16 v[92:95], v[40:43], v[124:127], v[92:95]
	v_mfma_f32_16x16x32_bf16 v[88:91], v[52:55], v[124:127], v[88:91]
	s_waitcnt lgkmcnt(5)
	v_mfma_f32_16x16x32_bf16 v[84:87], v[40:43], v[112:115], v[84:87]
	v_mfma_f32_16x16x32_bf16 v[112:115], v[52:55], v[112:115], v[76:79]
	s_waitcnt lgkmcnt(4)
	v_mfma_f32_16x16x32_bf16 v[72:75], v[40:43], v[80:83], v[72:75]
	v_mfma_f32_16x16x32_bf16 v[68:71], v[52:55], v[80:83], v[68:71]
	ds_read_b128 v[80:83], v195 offset:16384
	ds_read_b128 v[124:127], v195 offset:20480
	ds_read_b128 v[128:131], v195 offset:24576
	ds_read_b128 v[198:201], v195 offset:28672
	v_add_co_u32_e32 v214, vcc, s22, v186
	s_nop 1
	v_addc_co_u32_e32 v215, vcc, 0, v187, vcc
	global_load_dwordx4 v[40:43], v[186:187], off
	global_load_dwordx4 v[52:55], v[214:215], off
	ds_write_b128 v193, v[4:7] offset:32768
	s_waitcnt lgkmcnt(8)
	v_mfma_f32_16x16x32_bf16 v[4:7], v[28:31], v[160:163], v[136:139]
	s_waitcnt lgkmcnt(7)
	v_mfma_f32_16x16x32_bf16 v[120:123], v[28:31], v[156:159], v[120:123]
	s_waitcnt lgkmcnt(6)
	v_mfma_f32_16x16x32_bf16 v[108:111], v[28:31], v[152:155], v[108:111]
	s_waitcnt vmcnt(4)
	v_mfma_f32_16x16x32_bf16 v[104:107], v[48:51], v[152:155], v[104:107]
	s_waitcnt lgkmcnt(5)
	v_mfma_f32_16x16x32_bf16 v[136:139], v[28:31], v[148:151], v[140:143]
	v_mfma_f32_16x16x32_bf16 v[140:143], v[48:51], v[148:151], v[144:147]
	v_mfma_f32_16x16x32_bf16 v[132:135], v[48:51], v[160:163], v[132:135]
	v_mfma_f32_16x16x32_bf16 v[116:119], v[48:51], v[156:159], v[116:119]
	s_nop 0
	ds_read_b128 v[144:147], v196
	ds_read_b128 v[148:151], v196 offset:4096
	ds_read_b128 v[152:155], v196 offset:8192
	ds_read_b128 v[156:159], v196 offset:12288
	global_load_dwordx4 v[76:79], v[186:187], off offset:1024
	ds_write_b128 v193, v[8:11] offset:40960
	s_waitcnt lgkmcnt(9)
	v_mfma_f32_16x16x32_bf16 v[8:11], v[28:31], v[80:83], v[100:103]
	v_mfma_f32_16x16x32_bf16 v[80:83], v[48:51], v[80:83], v[96:99]
	s_waitcnt lgkmcnt(8)
	v_mfma_f32_16x16x32_bf16 v[92:95], v[28:31], v[124:127], v[92:95]
	v_mfma_f32_16x16x32_bf16 v[88:91], v[48:51], v[124:127], v[88:91]
	s_waitcnt lgkmcnt(7)
	v_mfma_f32_16x16x32_bf16 v[84:87], v[28:31], v[128:131], v[84:87]
	v_mfma_f32_16x16x32_bf16 v[96:99], v[48:51], v[128:131], v[112:115]
	s_waitcnt lgkmcnt(6)
	v_mfma_f32_16x16x32_bf16 v[28:31], v[28:31], v[198:201], v[72:75]
	v_mfma_f32_16x16x32_bf16 v[100:103], v[48:51], v[198:201], v[68:71]
	ds_read_b128 v[112:115], v196 offset:16384
	ds_read_b128 v[124:127], v196 offset:20480
	ds_read_b128 v[128:131], v196 offset:24576
	ds_read_b128 v[160:163], v196 offset:28672
	global_load_dwordx4 v[72:75], v[186:187], off offset:2048
	global_load_dwordx4 v[48:51], v[214:215], off offset:1024
	ds_write_b128 v193, v[12:15] offset:49152
	s_waitcnt lgkmcnt(8)
	v_mfma_f32_16x16x32_bf16 v[120:123], v[24:27], v[148:151], v[120:123]
	s_waitcnt lgkmcnt(7)
	v_mfma_f32_16x16x32_bf16 v[108:111], v[24:27], v[152:155], v[108:111]
	s_waitcnt vmcnt(6)
	v_mfma_f32_16x16x32_bf16 v[104:107], v[44:47], v[152:155], v[104:107]
	v_mfma_f32_16x16x32_bf16 v[4:7], v[24:27], v[144:147], v[4:7]
	v_mfma_f32_16x16x32_bf16 v[12:15], v[44:47], v[144:147], v[132:135]
	v_mfma_f32_16x16x32_bf16 v[116:119], v[44:47], v[148:151], v[116:119]
	s_waitcnt lgkmcnt(6)
	v_mfma_f32_16x16x32_bf16 v[132:135], v[24:27], v[156:159], v[136:139]
	v_mfma_f32_16x16x32_bf16 v[144:147], v[44:47], v[156:159], v[140:143]
	s_nop 1
	ds_read_b128 v[136:139], v197
	ds_read_b128 v[148:151], v197 offset:4096
	ds_read_b128 v[152:155], v197 offset:8192
	ds_read_b128 v[156:159], v197 offset:12288
	global_load_dwordx4 v[68:71], v[186:187], off offset:3072
	ds_write_b128 v193, v[16:19] offset:57344
	s_waitcnt lgkmcnt(9)
	v_mfma_f32_16x16x32_bf16 v[8:11], v[24:27], v[112:115], v[8:11]
	s_waitcnt lgkmcnt(8)
	v_mfma_f32_16x16x32_bf16 v[92:95], v[24:27], v[124:127], v[92:95]
	v_mfma_f32_16x16x32_bf16 v[88:91], v[44:47], v[124:127], v[88:91]
	s_waitcnt lgkmcnt(7)
	v_mfma_f32_16x16x32_bf16 v[84:87], v[24:27], v[128:131], v[84:87]
	s_waitcnt lgkmcnt(6)
	v_mfma_f32_16x16x32_bf16 v[24:27], v[24:27], v[160:163], v[28:31]
	v_mfma_f32_16x16x32_bf16 v[198:201], v[44:47], v[112:115], v[80:83]
	v_mfma_f32_16x16x32_bf16 v[128:131], v[44:47], v[128:131], v[96:99]
	v_mfma_f32_16x16x32_bf16 v[160:163], v[44:47], v[160:163], v[100:103]
	ds_read_b128 v[28:31], v197 offset:16384
	ds_read_b128 v[202:205], v197 offset:20480
	ds_read_b128 v[224:227], v197 offset:24576
	ds_read_b128 v[228:231], v197 offset:28672
	global_load_dwordx4 v[44:47], v[214:215], off offset:2048
	s_waitcnt lgkmcnt(8)
	v_mfma_f32_16x16x32_bf16 v[140:143], v[20:23], v[136:139], v[4:7]
	s_waitcnt vmcnt(7)
	v_mfma_f32_16x16x32_bf16 v[136:139], v[36:39], v[136:139], v[12:15]
	s_waitcnt lgkmcnt(7)
	v_mfma_f32_16x16x32_bf16 v[124:127], v[20:23], v[148:151], v[120:123]
	v_mfma_f32_16x16x32_bf16 v[120:123], v[36:39], v[148:151], v[116:119]
	s_waitcnt lgkmcnt(6)
	v_mfma_f32_16x16x32_bf16 v[112:115], v[20:23], v[152:155], v[108:111]
	v_mfma_f32_16x16x32_bf16 v[108:111], v[36:39], v[152:155], v[104:107]
	s_waitcnt lgkmcnt(5)
	v_mfma_f32_16x16x32_bf16 v[104:107], v[20:23], v[156:159], v[132:135]
	v_mfma_f32_16x16x32_bf16 v[16:19], v[36:39], v[156:159], v[144:147]
	global_load_dwordx4 v[80:83], v[214:215], off offset:3072
	s_waitcnt lgkmcnt(3)
	v_mfma_f32_16x16x32_bf16 v[100:103], v[20:23], v[28:31], v[8:11]
	v_mfma_f32_16x16x32_bf16 v[96:99], v[36:39], v[28:31], v[198:201]
	s_waitcnt lgkmcnt(2)
	v_mfma_f32_16x16x32_bf16 v[92:95], v[20:23], v[202:205], v[92:95]
	v_mfma_f32_16x16x32_bf16 v[88:91], v[36:39], v[202:205], v[88:91]
	s_waitcnt lgkmcnt(1)
	v_mfma_f32_16x16x32_bf16 v[84:87], v[20:23], v[224:227], v[84:87]
	v_mfma_f32_16x16x32_bf16 v[28:31], v[36:39], v[224:227], v[128:131]
	s_waitcnt lgkmcnt(0)
	v_mfma_f32_16x16x32_bf16 v[24:27], v[20:23], v[228:231], v[24:27]
	v_mfma_f32_16x16x32_bf16 v[20:23], v[36:39], v[228:231], v[160:163]
	s_cmp_eq_u32 s42, 1
	s_cselect_b64 s[0:1], -1, 0
	s_and_b64 s[0:1], s[0:1], s[38:39]
	s_andn2_b64 vcc, exec, s[0:1]
	s_cbranch_vccnz .LBB0_1574
	v_mov_b32_e32 v4, v192
	v_mov_b32_e32 v6, v167
	v_cvt_pk_bf16_f32 v5, v142, v143
	v_lshlrev_b32_e32 v7, 7, v4
	v_lshlrev_b32_e32 v6, 3, v6
	v_cvt_pk_bf16_f32 v4, v140, v141
	v_add3_u32 v8, s48, v7, v6
	v_cvt_pk_bf16_f32 v6, v136, v137
	v_cvt_pk_bf16_f32 v7, v138, v139
	ds_write2st64_b64 v8, v[4:5], v[6:7] offset1:1
	v_cvt_pk_bf16_f32 v4, v124, v125
	v_cvt_pk_bf16_f32 v5, v126, v127
	v_cvt_pk_bf16_f32 v6, v120, v121
	v_cvt_pk_bf16_f32 v7, v122, v123
	ds_write2st64_b64 v8, v[4:5], v[6:7] offset0:2 offset1:3
	v_cvt_pk_bf16_f32 v4, v112, v113
	v_cvt_pk_bf16_f32 v5, v114, v115
	v_cvt_pk_bf16_f32 v6, v108, v109
	v_cvt_pk_bf16_f32 v7, v110, v111
	ds_write2st64_b64 v8, v[4:5], v[6:7] offset0:4 offset1:5
	v_cvt_pk_bf16_f32 v4, v104, v105
	v_cvt_pk_bf16_f32 v5, v106, v107
	v_cvt_pk_bf16_f32 v6, v16, v17
	v_cvt_pk_bf16_f32 v7, v18, v19
	ds_write2st64_b64 v8, v[4:5], v[6:7] offset0:6 offset1:7
	v_cvt_pk_bf16_f32 v4, v100, v101
	v_cvt_pk_bf16_f32 v5, v102, v103
	v_cvt_pk_bf16_f32 v6, v96, v97
	v_cvt_pk_bf16_f32 v7, v98, v99
	ds_write2st64_b64 v8, v[4:5], v[6:7] offset0:8 offset1:9
	v_cvt_pk_bf16_f32 v4, v92, v93
	v_cvt_pk_bf16_f32 v5, v94, v95
	v_cvt_pk_bf16_f32 v6, v88, v89
	v_cvt_pk_bf16_f32 v7, v90, v91
	ds_write2st64_b64 v8, v[4:5], v[6:7] offset0:10 offset1:11
	v_cvt_pk_bf16_f32 v4, v84, v85
	v_cvt_pk_bf16_f32 v5, v86, v87
	v_cvt_pk_bf16_f32 v6, v28, v29
	v_cvt_pk_bf16_f32 v7, v30, v31
	ds_write2st64_b64 v8, v[4:5], v[6:7] offset0:12 offset1:13
	v_cvt_pk_bf16_f32 v6, v20, v21
	v_mov_b32_e32 v20, 0
	v_cvt_pk_bf16_f32 v4, v24, v25
	v_cvt_pk_bf16_f32 v5, v26, v27
	v_cvt_pk_bf16_f32 v7, v22, v23
	v_mov_b32_e32 v21, v20
	v_mov_b32_e32 v22, v20
	v_mov_b32_e32 v23, v20
	v_mov_b32_e32 v24, v20
	v_mov_b32_e32 v25, v20
	v_mov_b32_e32 v26, v20
	v_mov_b32_e32 v27, v20
	v_mov_b32_e32 v28, v20
	v_mov_b32_e32 v29, v20
	v_mov_b32_e32 v30, v20
	v_mov_b32_e32 v31, v20
	v_mov_b32_e32 v84, v20
	v_mov_b32_e32 v85, v20
	v_mov_b32_e32 v86, v20
	v_mov_b32_e32 v87, v20
	v_mov_b32_e32 v88, v20
	v_mov_b32_e32 v89, v20
	v_mov_b32_e32 v90, v20
	v_mov_b32_e32 v91, v20
	v_mov_b32_e32 v92, v20
	v_mov_b32_e32 v93, v20
	v_mov_b32_e32 v94, v20
	v_mov_b32_e32 v95, v20
	v_mov_b32_e32 v96, v20
	v_mov_b32_e32 v97, v20
	v_mov_b32_e32 v98, v20
	v_mov_b32_e32 v99, v20
	v_mov_b32_e32 v100, v20
	v_mov_b32_e32 v101, v20
	v_mov_b32_e32 v102, v20
	v_mov_b32_e32 v103, v20
	v_mov_b32_e32 v16, v20
	v_mov_b32_e32 v17, v20
	v_mov_b32_e32 v18, v20
	v_mov_b32_e32 v19, v20
	v_mov_b32_e32 v104, v20
	v_mov_b32_e32 v105, v20
	v_mov_b32_e32 v106, v20
	v_mov_b32_e32 v107, v20
	v_mov_b32_e32 v108, v20
	v_mov_b32_e32 v109, v20
	v_mov_b32_e32 v110, v20
	v_mov_b32_e32 v111, v20
	v_mov_b32_e32 v112, v20
	v_mov_b32_e32 v113, v20
	v_mov_b32_e32 v114, v20
	v_mov_b32_e32 v115, v20
	v_mov_b32_e32 v120, v20
	v_mov_b32_e32 v121, v20
	v_mov_b32_e32 v122, v20
	v_mov_b32_e32 v123, v20
	v_mov_b32_e32 v124, v20
	v_mov_b32_e32 v125, v20
	v_mov_b32_e32 v126, v20
	v_mov_b32_e32 v127, v20
	v_mov_b32_e32 v136, v20
	v_mov_b32_e32 v137, v20
	v_mov_b32_e32 v138, v20
	v_mov_b32_e32 v139, v20
	v_mov_b32_e32 v140, v20
	v_mov_b32_e32 v141, v20
	v_mov_b32_e32 v142, v20
	v_mov_b32_e32 v143, v20
	ds_write2st64_b64 v8, v[4:5], v[6:7] offset0:14 offset1:15

.LBB0_1584:
	ds_read_b128 v[152:155], v194 offset:32768
	ds_read_b128 v[148:151], v194 offset:36864
	ds_read_b128 v[144:147], v194 offset:40960
	ds_read_b128 v[12:15], v194 offset:45056
	ds_read_b128 v[132:135], v194 offset:49152
	ds_read_b128 v[128:131], v194 offset:53248
	ds_read_b128 v[116:119], v194 offset:57344
	ds_read_b128 v[36:39], v194 offset:61440
	s_add_i32 s12, s60, 1
	s_cmp_lg_u32 s12, 10
	s_cselect_b32 s60, s12, 0
	s_lshl_b32 s12, s60, 7
	s_add_i32 s42, s12, 0xfffffb00
	s_cmp_gt_i32 s60, 9
	s_cselect_b32 s12, s42, s12
	v_or_b32_e32 v186, s12, v165
	s_movk_i32 s12, 0xff
	v_cmp_lt_i32_e32 vcc, s12, v186
	v_mov_b32_e32 v187, v2
	s_nop 0
	v_cndmask_b32_e32 v4, v168, v178, vcc
	v_cndmask_b32_e32 v5, v169, v179, vcc
	v_lshl_add_u64 v[4:5], v[186:187], 1, v[4:5]
	global_load_dwordx4 v[4:7], v[4:5], off offset:-512
	v_cndmask_b32_e32 v8, v170, v180, vcc
	v_cndmask_b32_e32 v9, v171, v181, vcc
	v_lshl_add_u64 v[8:9], v[186:187], 1, v[8:9]
	global_load_dwordx4 v[8:11], v[8:9], off offset:-512
	s_waitcnt vmcnt(7) lgkmcnt(7)
	v_mfma_f32_16x16x32_bf16 v[140:143], v[40:43], v[152:155], v[140:143]
	s_waitcnt vmcnt(6)
	v_mfma_f32_16x16x32_bf16 v[136:139], v[52:55], v[152:155], v[136:139]
	s_waitcnt lgkmcnt(6)
	v_mfma_f32_16x16x32_bf16 v[124:127], v[40:43], v[148:151], v[124:127]
	v_mfma_f32_16x16x32_bf16 v[120:123], v[52:55], v[148:151], v[120:123]
	s_waitcnt lgkmcnt(5)
	v_mfma_f32_16x16x32_bf16 v[112:115], v[40:43], v[144:147], v[112:115]
	v_mfma_f32_16x16x32_bf16 v[108:111], v[52:55], v[144:147], v[108:111]
	s_waitcnt lgkmcnt(4)
	v_mfma_f32_16x16x32_bf16 v[104:107], v[40:43], v[12:15], v[104:107]
	v_mfma_f32_16x16x32_bf16 v[144:147], v[52:55], v[12:15], v[16:19]
	ds_read_b128 v[160:163], v195 offset:32768
	ds_read_b128 v[156:159], v195 offset:36864
	ds_read_b128 v[152:155], v195 offset:40960
	ds_read_b128 v[148:151], v195 offset:45056
	v_cndmask_b32_e32 v12, v172, v182, vcc
	v_cndmask_b32_e32 v13, v173, v183, vcc
	v_lshl_add_u64 v[12:13], v[186:187], 1, v[12:13]
	global_load_dwordx4 v[12:15], v[12:13], off offset:-512
	v_cndmask_b32_e32 v16, v174, v184, vcc
	v_cndmask_b32_e32 v17, v175, v185, vcc
	v_lshl_add_u64 v[16:17], v[186:187], 1, v[16:17]
	global_load_dwordx4 v[16:19], v[16:17], off offset:-512
	s_add_i32 s12, s62, s23
	s_add_i32 s42, s12, -4
	s_cmp_gt_i32 s12, 3
	s_cselect_b32 s12, s42, s12
	s_lshl_b32 s42, s61, 2
	s_sub_i32 s43, s42, 40
	s_cmp_gt_i32 s61, 9
	s_cselect_b32 s42, s43, s42
	s_mul_hi_i32 s61, s12, 0x280
	s_mulk_i32 s12, 0x280
	s_ashr_i32 s43, s42, 31
	s_add_u32 s42, s12, s42
	s_addc_u32 s43, s61, s43
	s_lshl_b64 s[42:43], s[42:43], 10
	v_lshl_add_u64 v[186:187], v[176:177], 0, s[42:43]
	s_waitcnt lgkmcnt(7)
	v_mfma_f32_16x16x32_bf16 v[100:103], v[40:43], v[132:135], v[100:103]
	v_mfma_f32_16x16x32_bf16 v[96:99], v[52:55], v[132:135], v[96:99]
	s_waitcnt lgkmcnt(6)
	v_mfma_f32_16x16x32_bf16 v[92:95], v[40:43], v[128:131], v[92:95]
	v_mfma_f32_16x16x32_bf16 v[88:91], v[52:55], v[128:131], v[88:91]
	s_waitcnt lgkmcnt(5)
	v_mfma_f32_16x16x32_bf16 v[84:87], v[40:43], v[116:119], v[84:87]
	v_mfma_f32_16x16x32_bf16 v[116:119], v[52:55], v[116:119], v[28:31]
	s_waitcnt lgkmcnt(4)
	v_mfma_f32_16x16x32_bf16 v[24:27], v[40:43], v[36:39], v[24:27]
	v_mfma_f32_16x16x32_bf16 v[20:23], v[52:55], v[36:39], v[20:23]
	ds_read_b128 v[36:39], v195 offset:49152
	ds_read_b128 v[128:131], v195 offset:53248
	ds_read_b128 v[132:135], v195 offset:57344
	ds_read_b128 v[198:201], v195 offset:61440
	v_add_co_u32_e32 v214, vcc, s22, v186
	s_nop 1
	v_addc_co_u32_e32 v215, vcc, 0, v187, vcc
	global_load_dwordx4 v[40:43], v[186:187], off
	global_load_dwordx4 v[52:55], v[214:215], off
	ds_write_b128 v193, v[32:35]
	s_waitcnt vmcnt(5) lgkmcnt(8)
	v_mfma_f32_16x16x32_bf16 v[136:139], v[48:51], v[160:163], v[136:139]
	s_waitcnt lgkmcnt(7)
	v_mfma_f32_16x16x32_bf16 v[120:123], v[48:51], v[156:159], v[120:123]
	s_waitcnt lgkmcnt(6)
	v_mfma_f32_16x16x32_bf16 v[108:111], v[48:51], v[152:155], v[108:111]
	s_waitcnt lgkmcnt(5)
	v_mfma_f32_16x16x32_bf16 v[104:107], v[76:79], v[148:151], v[104:107]
	v_mfma_f32_16x16x32_bf16 v[32:35], v[76:79], v[160:163], v[140:143]
	v_mfma_f32_16x16x32_bf16 v[124:127], v[76:79], v[156:159], v[124:127]
	v_mfma_f32_16x16x32_bf16 v[112:115], v[76:79], v[152:155], v[112:115]
	v_mfma_f32_16x16x32_bf16 v[140:143], v[48:51], v[148:151], v[144:147]
	s_nop 2
	ds_read_b128 v[144:147], v196 offset:32768
	ds_read_b128 v[148:151], v196 offset:36864
	ds_read_b128 v[152:155], v196 offset:40960
	ds_read_b128 v[156:159], v196 offset:45056
	global_load_dwordx4 v[28:31], v[186:187], off offset:1024
	ds_write_b128 v193, v[56:59] offset:8192
	s_waitcnt lgkmcnt(9)
	v_mfma_f32_16x16x32_bf16 v[56:59], v[76:79], v[36:39], v[100:103]
	v_mfma_f32_16x16x32_bf16 v[36:39], v[48:51], v[36:39], v[96:99]
	s_waitcnt lgkmcnt(8)
	v_mfma_f32_16x16x32_bf16 v[92:95], v[76:79], v[128:131], v[92:95]
	v_mfma_f32_16x16x32_bf16 v[88:91], v[48:51], v[128:131], v[88:91]
	s_waitcnt lgkmcnt(7)
	v_mfma_f32_16x16x32_bf16 v[84:87], v[76:79], v[132:135], v[84:87]
	v_mfma_f32_16x16x32_bf16 v[96:99], v[48:51], v[132:135], v[116:119]
	s_waitcnt lgkmcnt(6)
	v_mfma_f32_16x16x32_bf16 v[76:79], v[76:79], v[198:201], v[24:27]
	v_mfma_f32_16x16x32_bf16 v[100:103], v[48:51], v[198:201], v[20:23]
	ds_read_b128 v[116:119], v196 offset:49152
	ds_read_b128 v[128:131], v196 offset:53248
	ds_read_b128 v[132:135], v196 offset:57344
	ds_read_b128 v[160:163], v196 offset:61440
	global_load_dwordx4 v[24:27], v[186:187], off offset:2048
	global_load_dwordx4 v[48:51], v[214:215], off offset:1024
	ds_write_b128 v193, v[60:63] offset:16384
	s_waitcnt vmcnt(6) lgkmcnt(9)
	v_mfma_f32_16x16x32_bf16 v[60:63], v[44:47], v[144:147], v[136:139]
	v_mfma_f32_16x16x32_bf16 v[32:35], v[72:75], v[144:147], v[32:35]
	s_waitcnt lgkmcnt(8)
	v_mfma_f32_16x16x32_bf16 v[124:127], v[72:75], v[148:151], v[124:127]
	v_mfma_f32_16x16x32_bf16 v[144:147], v[44:47], v[148:151], v[120:123]
	s_waitcnt lgkmcnt(7)
	v_mfma_f32_16x16x32_bf16 v[112:115], v[72:75], v[152:155], v[112:115]
	v_mfma_f32_16x16x32_bf16 v[148:151], v[44:47], v[152:155], v[108:111]
	s_waitcnt lgkmcnt(6)
	v_mfma_f32_16x16x32_bf16 v[152:155], v[72:75], v[156:159], v[104:107]
	v_mfma_f32_16x16x32_bf16 v[140:143], v[44:47], v[156:159], v[140:143]
	s_nop 1
	ds_read_b128 v[104:107], v197 offset:32768
	ds_read_b128 v[108:111], v197 offset:36864
	ds_read_b128 v[156:159], v197 offset:40960
	ds_read_b128 v[198:201], v197 offset:45056
	global_load_dwordx4 v[20:23], v[186:187], off offset:3072
	ds_write_b128 v193, v[64:67] offset:24576
	s_waitcnt lgkmcnt(9)
	v_mfma_f32_16x16x32_bf16 v[56:59], v[72:75], v[116:119], v[56:59]
	s_waitcnt lgkmcnt(8)
	v_mfma_f32_16x16x32_bf16 v[92:95], v[72:75], v[128:131], v[92:95]
	v_mfma_f32_16x16x32_bf16 v[88:91], v[44:47], v[128:131], v[88:91]
	s_waitcnt lgkmcnt(7)
	v_mfma_f32_16x16x32_bf16 v[84:87], v[72:75], v[132:135], v[84:87]
	s_waitcnt lgkmcnt(6)
	v_mfma_f32_16x16x32_bf16 v[72:75], v[72:75], v[160:163], v[76:79]
	v_mfma_f32_16x16x32_bf16 v[202:205], v[44:47], v[116:119], v[36:39]
	v_mfma_f32_16x16x32_bf16 v[128:131], v[44:47], v[132:135], v[96:99]
	v_mfma_f32_16x16x32_bf16 v[160:163], v[44:47], v[160:163], v[100:103]
	ds_read_b128 v[76:79], v197 offset:49152
	ds_read_b128 v[224:227], v197 offset:53248
	ds_read_b128 v[228:231], v197 offset:57344
	ds_read_b128 v[232:235], v197 offset:61440
	global_load_dwordx4 v[44:47], v[214:215], off offset:2048
	s_waitcnt lgkmcnt(8)
	v_mfma_f32_16x16x32_bf16 v[136:139], v[68:71], v[104:107], v[32:35]
	s_waitcnt vmcnt(7)
	v_mfma_f32_16x16x32_bf16 v[132:135], v[80:83], v[104:107], v[60:63]
	s_waitcnt lgkmcnt(7)
	v_mfma_f32_16x16x32_bf16 v[120:123], v[68:71], v[108:111], v[124:127]
	v_mfma_f32_16x16x32_bf16 v[116:119], v[80:83], v[108:111], v[144:147]
	s_waitcnt lgkmcnt(6)
	v_mfma_f32_16x16x32_bf16 v[108:111], v[68:71], v[156:159], v[112:115]
	v_mfma_f32_16x16x32_bf16 v[104:107], v[80:83], v[156:159], v[148:151]
	s_waitcnt lgkmcnt(5)
	v_mfma_f32_16x16x32_bf16 v[64:67], v[68:71], v[198:201], v[152:155]
	v_mfma_f32_16x16x32_bf16 v[60:63], v[80:83], v[198:201], v[140:143]
	global_load_dwordx4 v[36:39], v[214:215], off offset:3072
	s_waitcnt lgkmcnt(3)
	v_mfma_f32_16x16x32_bf16 v[100:103], v[68:71], v[76:79], v[56:59]
	v_mfma_f32_16x16x32_bf16 v[96:99], v[80:83], v[76:79], v[202:205]
	s_waitcnt lgkmcnt(2)
	v_mfma_f32_16x16x32_bf16 v[92:95], v[68:71], v[224:227], v[92:95]
	v_mfma_f32_16x16x32_bf16 v[88:91], v[80:83], v[224:227], v[88:91]
	s_waitcnt lgkmcnt(1)
	v_mfma_f32_16x16x32_bf16 v[84:87], v[68:71], v[228:231], v[84:87]
	v_mfma_f32_16x16x32_bf16 v[76:79], v[80:83], v[228:231], v[128:131]
	s_waitcnt lgkmcnt(0)
	v_mfma_f32_16x16x32_bf16 v[72:75], v[68:71], v[232:235], v[72:75]
	v_mfma_f32_16x16x32_bf16 v[68:71], v[80:83], v[232:235], v[160:163]
	s_cmp_eq_u32 s63, 1
	s_cselect_b64 s[42:43], -1, 0
	s_and_b64 s[42:43], s[42:43], s[38:39]
	s_andn2_b64 vcc, exec, s[42:43]
	s_cbranch_vccnz .LBB0_1602
	v_mov_b32_e32 v32, v192
	v_mov_b32_e32 v34, v167
	v_cvt_pk_bf16_f32 v33, v138, v139
	v_lshlrev_b32_e32 v35, 7, v32
	v_lshlrev_b32_e32 v34, 3, v34
	v_cvt_pk_bf16_f32 v32, v136, v137
	v_add3_u32 v56, s48, v35, v34
	v_cvt_pk_bf16_f32 v34, v132, v133
	v_cvt_pk_bf16_f32 v35, v134, v135
	ds_write2st64_b64 v56, v[32:33], v[34:35] offset1:1
	v_cvt_pk_bf16_f32 v32, v120, v121
	v_cvt_pk_bf16_f32 v33, v122, v123
	v_cvt_pk_bf16_f32 v34, v116, v117
	v_cvt_pk_bf16_f32 v35, v118, v119
	ds_write2st64_b64 v56, v[32:33], v[34:35] offset0:2 offset1:3
	v_cvt_pk_bf16_f32 v32, v108, v109
	v_cvt_pk_bf16_f32 v33, v110, v111
	v_cvt_pk_bf16_f32 v34, v104, v105
	v_cvt_pk_bf16_f32 v35, v106, v107
	ds_write2st64_b64 v56, v[32:33], v[34:35] offset0:4 offset1:5
	v_cvt_pk_bf16_f32 v32, v64, v65
	v_cvt_pk_bf16_f32 v33, v66, v67
	v_cvt_pk_bf16_f32 v34, v60, v61
	v_cvt_pk_bf16_f32 v35, v62, v63
	ds_write2st64_b64 v56, v[32:33], v[34:35] offset0:6 offset1:7
	v_cvt_pk_bf16_f32 v32, v100, v101
	v_cvt_pk_bf16_f32 v33, v102, v103
	v_cvt_pk_bf16_f32 v34, v96, v97
	v_cvt_pk_bf16_f32 v35, v98, v99
	ds_write2st64_b64 v56, v[32:33], v[34:35] offset0:8 offset1:9
	v_cvt_pk_bf16_f32 v32, v92, v93
	v_cvt_pk_bf16_f32 v33, v94, v95
	v_cvt_pk_bf16_f32 v34, v88, v89
	v_cvt_pk_bf16_f32 v35, v90, v91
	ds_write2st64_b64 v56, v[32:33], v[34:35] offset0:10 offset1:11
	v_cvt_pk_bf16_f32 v32, v84, v85
	v_cvt_pk_bf16_f32 v33, v86, v87
	v_cvt_pk_bf16_f32 v34, v76, v77
	v_cvt_pk_bf16_f32 v35, v78, v79
	ds_write2st64_b64 v56, v[32:33], v[34:35] offset0:12 offset1:13
	v_cvt_pk_bf16_f32 v34, v68, v69
	v_mov_b32_e32 v68, 0
	v_cvt_pk_bf16_f32 v32, v72, v73
	v_cvt_pk_bf16_f32 v33, v74, v75
	v_cvt_pk_bf16_f32 v35, v70, v71
	v_mov_b32_e32 v69, v68
	v_mov_b32_e32 v70, v68
	v_mov_b32_e32 v71, v68
	v_mov_b32_e32 v72, v68
	v_mov_b32_e32 v73, v68
	v_mov_b32_e32 v74, v68
	v_mov_b32_e32 v75, v68
	v_mov_b32_e32 v76, v68
	v_mov_b32_e32 v77, v68
	v_mov_b32_e32 v78, v68
	v_mov_b32_e32 v79, v68
	v_mov_b32_e32 v84, v68
	v_mov_b32_e32 v85, v68
	v_mov_b32_e32 v86, v68
	v_mov_b32_e32 v87, v68
	v_mov_b32_e32 v88, v68
	v_mov_b32_e32 v89, v68
	v_mov_b32_e32 v90, v68
	v_mov_b32_e32 v91, v68
	v_mov_b32_e32 v92, v68
	v_mov_b32_e32 v93, v68
	v_mov_b32_e32 v94, v68
	v_mov_b32_e32 v95, v68
	v_mov_b32_e32 v96, v68
	v_mov_b32_e32 v97, v68
	v_mov_b32_e32 v98, v68
	v_mov_b32_e32 v99, v68
	v_mov_b32_e32 v100, v68
	v_mov_b32_e32 v101, v68
	v_mov_b32_e32 v102, v68
	v_mov_b32_e32 v103, v68
	v_mov_b32_e32 v60, v68
	v_mov_b32_e32 v61, v68
	v_mov_b32_e32 v62, v68
	v_mov_b32_e32 v63, v68
	v_mov_b32_e32 v64, v68
	v_mov_b32_e32 v65, v68
	v_mov_b32_e32 v66, v68
	v_mov_b32_e32 v67, v68
	v_mov_b32_e32 v104, v68
	v_mov_b32_e32 v105, v68
	v_mov_b32_e32 v106, v68
	v_mov_b32_e32 v107, v68
	v_mov_b32_e32 v108, v68
	v_mov_b32_e32 v109, v68
	v_mov_b32_e32 v110, v68
	v_mov_b32_e32 v111, v68
	v_mov_b32_e32 v116, v68
	v_mov_b32_e32 v117, v68
	v_mov_b32_e32 v118, v68
	v_mov_b32_e32 v119, v68
	v_mov_b32_e32 v120, v68
	v_mov_b32_e32 v121, v68
	v_mov_b32_e32 v122, v68
	v_mov_b32_e32 v123, v68
	v_mov_b32_e32 v132, v68
	v_mov_b32_e32 v133, v68
	v_mov_b32_e32 v134, v68
	v_mov_b32_e32 v135, v68
	v_mov_b32_e32 v136, v68
	v_mov_b32_e32 v137, v68
	v_mov_b32_e32 v138, v68
	v_mov_b32_e32 v139, v68
	ds_write2st64_b64 v56, v[32:33], v[34:35] offset0:14 offset1:15
